# hgrn level-3 loop: the 4 loop-invariant norm-gamma loads hoisted out of the chunk loop
# speedup vs baseline: 1.0079x; 1.0001x over previous
.LBB0_499:
.LBB0_500:
	s_add_u32 s26, s50, 0x587d0000
	s_waitcnt vmcnt(0)
	v_lshrrev_b32_e32 v95, 3, v0
	v_readlane_b32 s33, v237, 37
	v_lshlrev_b32_e32 v9, 6, v0
	s_movk_i32 s1, 0x204
	s_addc_u32 s27, s51, 0
	v_and_b32_e32 v3, 7, v0
	v_lshlrev_b32_e32 v2, 1, v0
	v_lshrrev_b32_e32 v7, 2, v0
	v_and_b32_e32 v6, 0x7f, v0
	s_add_i32 s0, 0, 0x1bc00
	v_and_b32_e32 v9, 0x1c0, v9
	v_mad_u32_u24 v10, v95, s1, 0
	s_lshl_b32 s7, s33, 3
	v_and_b32_e32 v92, 15, v0
	v_and_b32_e32 v96, 62, v2
	v_and_b32_e32 v2, 0x78, v7
	v_lshlrev_b32_e32 v8, 2, v0
	v_add_u32_e32 v98, s0, v9
	v_add_u32_e32 v99, v10, v9
	v_lshlrev_b32_e32 v9, 2, v6
	v_lshlrev_b32_e32 v6, 6, v3
	v_or_b32_e32 v7, 7, v7
	s_and_b32 s7, s7, 0x1ffffff0
	v_add_u32_e32 v97, s0, v8
	v_add_u32_e32 v102, s0, v6
	s_movk_i32 s0, 0x110
	v_mul_u32_u24_e32 v16, 0x90, v7
	v_or_b32_e32 v7, s7, v92
	s_add_i32 s1, 0, 0x10c00
	s_lshl_b32 s6, s33, 5
	v_mul_lo_u32 v7, v7, s0
	v_lshlrev_b32_e32 v93, 2, v1
	v_mov_b32_e32 v13, s1
	v_add_u32_e32 v17, 0, v7
	v_or_b32_e32 v7, s7, v93
	v_and_or_b32 v18, s6, 32, v92
	v_add_u32_e32 v103, v10, v6
	v_mad_u32_u24 v10, v95, s0, 0
	v_mad_u32_u24 v14, v95, s0, v13
	v_mad_u32_u24 v113, v18, s0, v13
	s_add_i32 s0, 0, 0x19800
	v_or_b32_e32 v20, 1, v7
	v_or_b32_e32 v21, 2, v7
	v_or_b32_e32 v22, 3, v7
	v_lshl_or_b32 v54, s33, 4, v92
	s_movk_i32 s29, 0x90
	v_lshl_add_u32 v13, v18, 1, s0
	v_cmp_gt_u32_e64 s[6:7], v18, v7
	v_cmp_gt_u32_e64 s[8:9], v18, v20
	v_cmp_gt_u32_e64 s[10:11], v18, v21
	v_cmp_gt_u32_e64 s[12:13], v18, v22
	v_or_b32_e32 v18, 16, v18
	s_add_i32 s1, 0, 0x15000
	v_and_b32_e32 v112, 48, v0
	v_mul_lo_u32 v19, v7, s29
	v_cmp_gt_u32_e64 s[14:15], v18, v7
	v_mul_lo_u32 v7, v54, s29
	s_mov_b64 s[90:91], s[86:87]
	v_mov_b32_e32 v55, 0
	v_lshl_add_u32 v24, v18, 1, s0
	v_cmp_gt_u32_e64 s[16:17], v18, v20
	v_cmp_gt_u32_e64 s[18:19], v18, v21
	v_cmp_gt_u32_e64 s[20:21], v18, v22
	v_add_u32_e32 v18, s1, v7
	v_add_u32_e32 v20, s0, v112
	s_lshl_b32 s0, s33, 6
	v_or_b32_e32 v7, 48, v194
	v_readlane_b32 s72, v237, 21
	v_and_b32_e32 v4, 48, v194
	v_mov_b32_e32 v5, v55
	s_add_i32 s3, 0, 0x1be00
	s_add_i32 s0, s0, 0
	v_mul_u32_u24_e32 v26, 0x90, v7
	v_mul_u32_u24_e32 v27, 0x110, v7
	v_mov_b32_e32 v7, v55
	v_readlane_b32 s76, v237, 25
	v_readlane_b32 s77, v237, 26
	v_lshl_add_u64 v[4:5], s[50:51], 0, v[4:5]
	v_lshrrev_b32_e32 v100, 7, v0
	v_add_u32_e32 v101, s3, v8
	v_add_u32_e32 v104, 0, v6
	v_and_b32_e32 v8, 0x7c, v8
	v_lshl_add_u32 v21, v92, 2, s0
	s_movk_i32 s0, 0x210
	v_lshl_add_u64 v[56:57], s[76:77], 0, v[6:7]
	v_lshlrev_b64 v[6:7], 8, v[54:55]
	v_lshlrev_b32_e32 v52, 4, v3
	v_add_u32_e32 v11, 0, v9
	v_mul_u32_u24_e32 v12, 0x2040, v100
	v_lshlrev_b32_e32 v3, 5, v3
	v_add_u32_e32 v8, s1, v8
	v_mul_u32_u24_e32 v15, 0x90, v2
	v_add_u32_e32 v23, 0x1100, v113
	v_add_u32_e32 v114, 0, v112
	v_mul_u32_u24_e32 v22, 0x90, v92
	v_mul_u32_u24_e32 v25, 0x840, v1
	v_mad_u32_u24 v115, v95, s0, v104
	v_readlane_b32 s80, v237, 29
	v_readlane_b32 s82, v237, 31
	v_readlane_b32 s83, v237, 32
	v_lshl_add_u64 v[4:5], v[4:5], 0, v[6:7]
	s_mov_b64 s[0:1], 0x4e6d0000
	v_lshlrev_b32_e32 v60, 1, v2
	v_mbcnt_lo_u32_b32 v2, -1, 0
	s_mov_b64 s[92:93], s[60:61]
	v_mov_b32_e32 v53, v55
	v_lshlrev_b32_e32 v50, 3, v1
	v_mov_b32_e32 v51, v55
	s_mov_b32 s61, 0
	v_add_u32_e32 v105, 8, v102
	v_add_u32_e32 v106, 16, v102
	v_add_u32_e32 v107, 24, v102
	v_add_u32_e32 v108, 32, v102
	v_add_u32_e32 v109, 40, v102
	v_add_u32_e32 v110, 48, v102
	v_add_u32_e32 v111, 56, v102
	v_mul_u32_u24_e32 v94, 0x110, v92
	v_lshl_add_u64 v[58:59], v[4:5], 0, s[0:1]
	v_add_u32_e32 v116, s3, v9
	s_movk_i32 s3, 0x5600
	v_lshlrev_b32_e32 v54, 1, v52
	s_mov_b64 s[56:57], 0x1e00
	s_mov_b64 s[82:83], 0x2e00
	s_mov_b32 s29, 0x3fb8aa3b
	s_mov_b32 s33, 0xc2ce8ed0
	s_mov_b32 s34, 0x42b17218
	s_mov_b32 s35, 0x7f800000
	s_mov_b32 s54, 0x800000
	s_mov_b32 s55, 0x3f317217
	s_mov_b32 s58, 0xffff0000
	v_add_u32_e32 v117, v10, v3
	v_add_u32_e32 v118, v14, v3
	v_add_u32_e32 v119, v8, v15
	v_add_u32_e32 v120, v8, v16
	v_add_u32_e32 v121, v17, v112
	s_movk_i32 s59, 0x7fff
	v_add_u32_e32 v122, v13, v19
	v_add_u32_e32 v123, v23, v112
	v_add_u32_e32 v124, v24, v19
	v_add_u32_e32 v125, v18, v112
	v_add_u32_e32 v126, v20, v22
	v_add_u32_e32 v127, v21, v25
	v_add_u32_e32 v128, v20, v26
	v_add_u32_e32 v129, v114, v27
	v_mov_b32_e32 v130, 0x3727c5ac
	v_mov_b32_e32 v131, 0x7f800000
	v_mov_b32_e32 v132, 0x41b17218
	v_add_u32_e32 v133, v11, v12
	v_mbcnt_hi_u32_b32 v134, -1, v2
	s_mov_b32 s80, s2
	v_readlane_b32 s73, v237, 22
	v_readlane_b32 s74, v237, 23
	v_readlane_b32 s75, v237, 24
	v_readlane_b32 s78, v237, 27
	v_readlane_b32 s79, v237, 28
	v_readlane_b32 s81, v237, 30
	v_readlane_b32 s84, v237, 33
	v_readlane_b32 s85, v237, 34
	v_readlane_b32 s86, v237, 35
	v_readlane_b32 s87, v237, 36
	global_load_dwordx4 v[238:241], v[56:57], off offset:48
	global_load_dwordx4 v[242:245], v[56:57], off offset:32
	global_load_dwordx4 v[246:249], v[56:57], off offset:16
	global_load_dwordx4 v[250:253], v[56:57], off
	s_waitcnt vmcnt(0)
	s_branch .LBB0_502
.LBB0_501:
	s_or_b64 exec, exec, s[0:1]
	v_add_f32_e32 v89, v89, v135
	v_add_f32_e32 v91, v91, v135
	ds_write2_b32 v61, v89, v91 offset0:2 offset1:131
	v_add_f32_e32 v61, v85, v135
	v_add_f32_e32 v85, v87, v135
	ds_write2_b32 v49, v61, v85 offset0:4 offset1:133
	v_add_f32_e32 v49, v81, v135
	v_add_f32_e32 v61, v83, v135
	ds_write2_b32 v47, v49, v61 offset0:6 offset1:135
	v_add_f32_e32 v47, v77, v135
	v_add_f32_e32 v49, v79, v135
	ds_write2_b32 v45, v47, v49 offset0:8 offset1:137
	v_add_f32_e32 v45, v73, v135
	v_add_f32_e32 v47, v75, v135
	ds_write2_b32 v44, v45, v47 offset0:10 offset1:139
	v_add_f32_e32 v44, v69, v135
	v_add_f32_e32 v45, v71, v135
	v_add_f32_e32 v136, v136, v135
	v_add_f32_e32 v137, v137, v135
	ds_write2_b32 v43, v44, v45 offset0:12 offset1:141
	v_add_f32_e32 v43, v65, v135
	v_add_f32_e32 v44, v67, v135
	ds_write2_b32 v133, v136, v137 offset1:129
	ds_write2_b32 v42, v43, v44 offset0:14 offset1:143
	s_waitcnt lgkmcnt(0)
	s_barrier
	s_waitcnt vmcnt(8)
	v_and_b32_e32 v49, 0xffff0000, v38
	v_lshlrev_b32_e32 v38, 16, v38
	v_add_u32_e32 v47, 0x3e7c, v104
	ds_read_b64 v[42:43], v102
	ds_read2_b32 v[44:45], v103 offset1:1
	ds_read2_b32 v[136:137], v47 offset1:1
	v_mul_f32_e32 v47, 0xbfb8aa3b, v38
	v_exp_f32_e32 v47, v47
	s_waitcnt lgkmcnt(2)
	v_mov_b32_e32 v87, v42
	s_waitcnt lgkmcnt(1)
	v_mul_f32_e32 v61, 0x3fb8aa3b, v44
	s_waitcnt lgkmcnt(0)
	v_sub_f32_e32 v65, v44, v136
	v_sub_f32_e32 v44, v136, v44
	v_add_f32_e32 v47, 1.0, v47
	v_mul_f32_e32 v44, 0x3fb8aa3b, v44
	v_rcp_f32_e32 v47, v47
	v_mul_f32_e32 v65, 0x3fb8aa3b, v65
	v_exp_f32_e32 v44, v44
	v_exp_f32_e32 v61, v61
	v_exp_f32_e32 v65, v65
	v_pk_add_f32 v[86:87], v[86:87], 1.0 op_sel_hi:[1,0] neg_lo:[1,0] neg_hi:[1,0]
	v_mul_f32_e32 v38, v47, v38
	v_mul_f32_e32 v42, v86, v87
	v_mul_f32_e32 v44, v42, v44
	v_mul_f32_e32 v42, 0xbfb8aa3b, v49
	v_mul_f32_e32 v61, v38, v61
	v_mul_f32_e32 v38, v38, v65
	v_exp_f32_e32 v65, v42
	v_mov_b32_e32 v47, v43
	v_pk_add_f32 v[42:43], v[46:47], 1.0 op_sel_hi:[1,0] neg_lo:[1,0] neg_hi:[1,0]
	v_sub_f32_e32 v47, v45, v137
	v_mul_f32_e32 v42, v42, v43
	v_add_f32_e32 v43, 1.0, v65
	v_rcp_f32_e32 v43, v43
	v_mul_f32_e32 v46, 0x3fb8aa3b, v45
	v_mul_f32_e32 v47, 0x3fb8aa3b, v47
	v_sub_f32_e32 v45, v137, v45
	v_exp_f32_e32 v46, v46
	v_exp_f32_e32 v47, v47
	v_mul_f32_e32 v45, 0x3fb8aa3b, v45
	v_exp_f32_e32 v45, v45
	v_mul_f32_e32 v43, v43, v49
	v_mul_f32_e32 v46, v43, v46
	v_mul_f32_e32 v43, v43, v47
	v_mul_f32_e32 v45, v42, v45
	v_cvt_pk_bf16_f32 v46, v61, v46
	v_cvt_pk_bf16_f32 v42, v38, v43
	v_and_b32_e32 v43, 0xffff0000, v39
	v_lshlrev_b32_e32 v39, 16, v39
	v_add_u32_e32 v47, 0x3e84, v104
	v_cvt_pk_bf16_f32 v38, v44, v45
	ds_read_b64 v[44:45], v105
	ds_read2_b32 v[86:87], v47 offset1:1
	ds_read2_b32 v[136:137], v103 offset0:2 offset1:3
	v_mul_f32_e32 v47, 0xbfb8aa3b, v39
	v_exp_f32_e32 v47, v47
	s_waitcnt lgkmcnt(2)
	v_mov_b32_e32 v89, v44
	v_pk_add_f32 v[88:89], v[88:89], 1.0 op_sel_hi:[1,0] neg_lo:[1,0] neg_hi:[1,0]
	s_waitcnt lgkmcnt(0)
	v_sub_f32_e32 v65, v86, v136
	v_add_f32_e32 v47, 1.0, v47
	v_rcp_f32_e32 v47, v47
	v_mul_f32_e32 v49, 0x3fb8aa3b, v136
	v_sub_f32_e32 v61, v136, v86
	v_mul_f32_e32 v65, 0x3fb8aa3b, v65
	v_exp_f32_e32 v49, v49
	v_mul_f32_e32 v61, 0x3fb8aa3b, v61
	v_exp_f32_e32 v65, v65
	v_exp_f32_e32 v61, v61
	v_mul_f32_e32 v44, v88, v89
	v_mul_f32_e32 v39, v47, v39
	v_mul_f32_e32 v47, v39, v49
	v_mul_f32_e32 v49, v44, v65
	v_mul_f32_e32 v44, 0xbfb8aa3b, v43
	v_mul_f32_e32 v39, v39, v61
	v_exp_f32_e32 v61, v44
	v_mov_b32_e32 v91, v45
	v_pk_add_f32 v[44:45], v[90:91], 1.0 op_sel_hi:[1,0] neg_lo:[1,0] neg_hi:[1,0]
	v_sub_f32_e32 v65, v137, v87
	v_mul_f32_e32 v44, v44, v45
	v_add_f32_e32 v45, 1.0, v61
	v_rcp_f32_e32 v45, v45
	v_mul_f32_e32 v61, 0x3fb8aa3b, v137
	v_mul_f32_e32 v65, 0x3fb8aa3b, v65
	v_sub_f32_e32 v67, v87, v137
	v_exp_f32_e32 v61, v61
	v_exp_f32_e32 v65, v65
	v_mul_f32_e32 v67, 0x3fb8aa3b, v67
	v_exp_f32_e32 v67, v67
	v_mul_f32_e32 v43, v45, v43
	v_mul_f32_e32 v45, v43, v61
	v_mul_f32_e32 v43, v43, v65
	v_mul_f32_e32 v44, v44, v67
	v_cvt_pk_bf16_f32 v47, v47, v45
	v_cvt_pk_bf16_f32 v43, v39, v43
	v_cvt_pk_bf16_f32 v39, v49, v44
	v_and_b32_e32 v61, 0xffff0000, v40
	v_lshlrev_b32_e32 v40, 16, v40
	v_add_u32_e32 v49, 0x3e8c, v104
	ds_read_b64 v[44:45], v106
	ds_read2_b32 v[86:87], v49 offset1:1
	ds_read2_b32 v[88:89], v103 offset0:4 offset1:5
	v_mul_f32_e32 v49, 0xbfb8aa3b, v40
	v_exp_f32_e32 v49, v49
	s_waitcnt lgkmcnt(2)
	v_mov_b32_e32 v85, v44
	v_pk_add_f32 v[84:85], v[84:85], 1.0 op_sel_hi:[1,0] neg_lo:[1,0] neg_hi:[1,0]
	s_waitcnt lgkmcnt(0)
	v_sub_f32_e32 v67, v88, v86
	v_add_f32_e32 v49, 1.0, v49
	v_sub_f32_e32 v69, v86, v88
	v_rcp_f32_e32 v49, v49
	v_mul_f32_e32 v65, 0x3fb8aa3b, v88
	v_mul_f32_e32 v67, 0x3fb8aa3b, v67
	v_mul_f32_e32 v69, 0x3fb8aa3b, v69
	v_exp_f32_e32 v65, v65
	v_exp_f32_e32 v67, v67
	v_exp_f32_e32 v69, v69
	v_mul_f32_e32 v44, v84, v85
	v_mul_f32_e32 v40, v49, v40
	v_mul_f32_e32 v65, v40, v65
	v_mul_f32_e32 v40, v40, v67
	v_mul_f32_e32 v67, v44, v69
	v_mul_f32_e32 v44, 0xbfb8aa3b, v61
	v_exp_f32_e32 v69, v44
	v_mov_b32_e32 v49, v45
	v_pk_add_f32 v[44:45], v[48:49], 1.0 op_sel_hi:[1,0] neg_lo:[1,0] neg_hi:[1,0]
	v_sub_f32_e32 v49, v89, v87
	v_mul_f32_e32 v44, v44, v45
	v_add_f32_e32 v45, 1.0, v69
	v_sub_f32_e32 v69, v87, v89
	v_rcp_f32_e32 v45, v45
	v_mul_f32_e32 v48, 0x3fb8aa3b, v89
	v_mul_f32_e32 v49, 0x3fb8aa3b, v49
	v_mul_f32_e32 v69, 0x3fb8aa3b, v69
	v_exp_f32_e32 v48, v48
	v_exp_f32_e32 v49, v49
	v_exp_f32_e32 v69, v69
	v_mul_f32_e32 v45, v45, v61
	v_mul_f32_e32 v48, v45, v48
	v_mul_f32_e32 v45, v45, v49
	v_mul_f32_e32 v49, v44, v69
	v_cvt_pk_bf16_f32 v48, v65, v48
	v_cvt_pk_bf16_f32 v44, v40, v45
	v_cvt_pk_bf16_f32 v40, v67, v49
	v_and_b32_e32 v45, 0xffff0000, v41
	v_lshlrev_b32_e32 v41, 16, v41
	v_add_u32_e32 v49, 0x3e94, v104
	ds_read_b64 v[84:85], v107
	ds_read2_b32 v[86:87], v49 offset1:1
	ds_read2_b32 v[88:89], v103 offset0:6 offset1:7
	v_mul_f32_e32 v49, 0xbfb8aa3b, v41
	v_exp_f32_e32 v49, v49
	s_waitcnt lgkmcnt(2)
	v_mov_b32_e32 v81, v84
	v_pk_add_f32 v[80:81], v[80:81], 1.0 op_sel_hi:[1,0] neg_lo:[1,0] neg_hi:[1,0]
	s_waitcnt lgkmcnt(0)
	v_mul_f32_e32 v65, 0x3fb8aa3b, v88
	v_add_f32_e32 v49, 1.0, v49
	v_rcp_f32_e32 v49, v49
	v_exp_f32_e32 v65, v65
	v_sub_f32_e32 v69, v86, v88
	v_mul_f32_e32 v69, 0x3fb8aa3b, v69
	v_mul_f32_e32 v41, v49, v41
	v_mul_f32_e32 v49, v41, v65
	v_mul_f32_e32 v65, 0xbfb8aa3b, v45
	v_exp_f32_e32 v65, v65
	v_exp_f32_e32 v69, v69
	v_mul_f32_e32 v61, v80, v81
	v_sub_f32_e32 v67, v88, v86
	v_add_f32_e32 v65, 1.0, v65
	v_sub_f32_e32 v71, v89, v87
	v_mul_f32_e32 v67, 0x3fb8aa3b, v67
	v_mul_f32_e32 v61, v61, v69
	v_rcp_f32_e32 v65, v65
	v_mul_f32_e32 v69, 0x3fb8aa3b, v89
	v_mul_f32_e32 v71, 0x3fb8aa3b, v71
	v_sub_f32_e32 v73, v87, v89
	v_exp_f32_e32 v67, v67
	v_exp_f32_e32 v69, v69
	v_exp_f32_e32 v71, v71
	v_mul_f32_e32 v73, 0x3fb8aa3b, v73
	v_exp_f32_e32 v73, v73
	v_mov_b32_e32 v83, v85
	v_pk_add_f32 v[80:81], v[82:83], 1.0 op_sel_hi:[1,0] neg_lo:[1,0] neg_hi:[1,0]
	v_mul_f32_e32 v45, v65, v45
	v_mul_f32_e32 v41, v41, v67
	v_mul_f32_e32 v67, v80, v81
	v_mul_f32_e32 v65, v45, v69
	v_mul_f32_e32 v45, v45, v71
	v_mul_f32_e32 v67, v67, v73
	v_cvt_pk_bf16_f32 v49, v49, v65
	v_cvt_pk_bf16_f32 v45, v41, v45
	v_cvt_pk_bf16_f32 v41, v61, v67
	v_and_b32_e32 v61, 0xffff0000, v34
	v_lshlrev_b32_e32 v34, 16, v34
	v_add_u32_e32 v65, 0x3e9c, v104
	ds_read_b64 v[80:81], v108
	ds_read2_b32 v[82:83], v65 offset1:1
	ds_read2_b32 v[84:85], v103 offset0:8 offset1:9
	v_mul_f32_e32 v65, 0xbfb8aa3b, v34
	v_exp_f32_e32 v65, v65
	s_waitcnt lgkmcnt(2)
	v_mov_b32_e32 v77, v80
	v_pk_add_f32 v[76:77], v[76:77], 1.0 op_sel_hi:[1,0] neg_lo:[1,0] neg_hi:[1,0]
	s_waitcnt lgkmcnt(0)
	v_sub_f32_e32 v71, v84, v82
	v_add_f32_e32 v65, 1.0, v65
	v_rcp_f32_e32 v65, v65
	v_mul_f32_e32 v69, 0x3fb8aa3b, v84
	v_mul_f32_e32 v71, 0x3fb8aa3b, v71
	v_exp_f32_e32 v69, v69
	v_exp_f32_e32 v71, v71
	v_mul_f32_e32 v34, v65, v34
	v_sub_f32_e32 v73, v82, v84
	v_mul_f32_e32 v65, v34, v69
	v_mul_f32_e32 v69, v34, v71
	v_mul_f32_e32 v34, 0xbfb8aa3b, v61
	v_mul_f32_e32 v73, 0x3fb8aa3b, v73
	v_exp_f32_e32 v34, v34
	v_exp_f32_e32 v73, v73
	v_mul_f32_e32 v67, v76, v77
	v_mov_b32_e32 v79, v81
	v_add_f32_e32 v34, 1.0, v34
	v_mul_f32_e32 v67, v67, v73
	v_pk_add_f32 v[76:77], v[78:79], 1.0 op_sel_hi:[1,0] neg_lo:[1,0] neg_hi:[1,0]
	v_rcp_f32_e32 v34, v34
	v_mul_f32_e32 v73, 0x3fb8aa3b, v85
	v_sub_f32_e32 v75, v85, v83
	v_mul_f32_e32 v71, v76, v77
	v_exp_f32_e32 v73, v73
	v_mul_f32_e32 v75, 0x3fb8aa3b, v75
	v_sub_f32_e32 v76, v83, v85
	v_exp_f32_e32 v75, v75
	v_mul_f32_e32 v76, 0x3fb8aa3b, v76
	v_exp_f32_e32 v76, v76
	v_mul_f32_e32 v34, v34, v61
	v_mul_f32_e32 v61, v34, v73
	v_mul_f32_e32 v73, v34, v75
	v_cvt_pk_bf16_f32 v34, v65, v61
	v_and_b32_e32 v61, 0xffff0000, v35
	v_lshlrev_b32_e32 v35, 16, v35
	v_add_u32_e32 v65, 0x3ea4, v104
	v_mul_f32_e32 v71, v71, v76
	v_cvt_pk_bf16_f32 v76, v69, v73
	v_cvt_pk_bf16_f32 v80, v67, v71
	ds_read_b64 v[78:79], v109
	ds_read2_b32 v[82:83], v65 offset1:1
	ds_read2_b32 v[84:85], v103 offset0:10 offset1:11
	v_mul_f32_e32 v65, 0xbfb8aa3b, v35
	v_exp_f32_e32 v65, v65
	s_waitcnt lgkmcnt(2)
	v_mov_b32_e32 v73, v78
	v_pk_add_f32 v[72:73], v[72:73], 1.0 op_sel_hi:[1,0] neg_lo:[1,0] neg_hi:[1,0]
	s_waitcnt lgkmcnt(0)
	v_sub_f32_e32 v71, v84, v82
	v_add_f32_e32 v65, 1.0, v65
	v_rcp_f32_e32 v65, v65
	v_mul_f32_e32 v69, 0x3fb8aa3b, v84
	v_mul_f32_e32 v71, 0x3fb8aa3b, v71
	v_exp_f32_e32 v69, v69
	v_exp_f32_e32 v71, v71
	v_mul_f32_e32 v67, v72, v73
	v_sub_f32_e32 v72, v82, v84
	v_mul_f32_e32 v35, v65, v35
	v_mul_f32_e32 v72, 0x3fb8aa3b, v72
	v_mul_f32_e32 v65, v35, v69
	v_mul_f32_e32 v69, v35, v71
	v_mul_f32_e32 v35, 0xbfb8aa3b, v61
	v_exp_f32_e32 v72, v72
	v_exp_f32_e32 v35, v35
	v_mov_b32_e32 v75, v79
	v_ashrrev_i32_e32 v63, 31, v62
	v_mul_f32_e32 v67, v67, v72
	v_pk_add_f32 v[72:73], v[74:75], 1.0 op_sel_hi:[1,0] neg_lo:[1,0] neg_hi:[1,0]
	v_add_f32_e32 v35, 1.0, v35
	v_mul_f32_e32 v71, v72, v73
	v_rcp_f32_e32 v35, v35
	v_mul_f32_e32 v72, 0x3fb8aa3b, v85
	v_sub_f32_e32 v73, v85, v83
	v_exp_f32_e32 v72, v72
	v_mul_f32_e32 v73, 0x3fb8aa3b, v73
	v_sub_f32_e32 v74, v83, v85
	v_exp_f32_e32 v73, v73
	v_mul_f32_e32 v74, 0x3fb8aa3b, v74
	v_exp_f32_e32 v74, v74
	v_mul_f32_e32 v35, v35, v61
	v_mul_f32_e32 v61, v35, v72
	v_mul_f32_e32 v72, v35, v73
	v_cvt_pk_bf16_f32 v35, v65, v61
	v_and_b32_e32 v61, 0xffff0000, v36
	v_lshlrev_b32_e32 v36, 16, v36
	v_add_u32_e32 v65, 0x3eac, v104
	v_mul_f32_e32 v71, v71, v74
	v_cvt_pk_bf16_f32 v77, v69, v72
	v_cvt_pk_bf16_f32 v81, v67, v71
	ds_read_b64 v[72:73], v110
	ds_read2_b32 v[74:75], v65 offset1:1
	ds_read2_b32 v[78:79], v103 offset0:12 offset1:13
	v_mul_f32_e32 v65, 0xbfb8aa3b, v36
	v_exp_f32_e32 v65, v65
	s_waitcnt lgkmcnt(2)
	v_mov_b32_e32 v69, v72
	v_pk_add_f32 v[68:69], v[68:69], 1.0 op_sel_hi:[1,0] neg_lo:[1,0] neg_hi:[1,0]
	s_waitcnt lgkmcnt(0)
	v_sub_f32_e32 v71, v74, v78
	v_mul_f32_e32 v67, v68, v69
	v_add_f32_e32 v65, 1.0, v65
	v_sub_f32_e32 v69, v78, v74
	v_rcp_f32_e32 v65, v65
	v_mul_f32_e32 v68, 0x3fb8aa3b, v78
	v_mul_f32_e32 v69, 0x3fb8aa3b, v69
	v_exp_f32_e32 v68, v68
	v_exp_f32_e32 v69, v69
	v_mul_f32_e32 v71, 0x3fb8aa3b, v71
	v_mul_f32_e32 v36, v65, v36
	v_exp_f32_e32 v71, v71
	v_mul_f32_e32 v65, v36, v68
	v_mul_f32_e32 v72, v36, v69
	v_mul_f32_e32 v36, 0xbfb8aa3b, v61
	v_exp_f32_e32 v36, v36
	v_mul_f32_e32 v67, v67, v71
	v_mov_b32_e32 v71, v73
	v_pk_add_f32 v[68:69], v[70:71], 1.0 op_sel_hi:[1,0] neg_lo:[1,0] neg_hi:[1,0]
	v_add_f32_e32 v36, 1.0, v36
	v_mul_f32_e32 v68, v68, v69
	v_rcp_f32_e32 v36, v36
	v_mul_f32_e32 v69, 0x3fb8aa3b, v79
	v_sub_f32_e32 v70, v79, v75
	v_sub_f32_e32 v71, v75, v79
	v_exp_f32_e32 v69, v69
	v_mul_f32_e32 v70, 0x3fb8aa3b, v70
	v_mul_f32_e32 v71, 0x3fb8aa3b, v71
	v_exp_f32_e32 v70, v70
	v_exp_f32_e32 v71, v71
	v_mul_f32_e32 v36, v36, v61
	v_mul_f32_e32 v61, v36, v69
	v_mul_f32_e32 v69, v36, v70
	v_mul_f32_e32 v68, v68, v71
	v_cvt_pk_bf16_f32 v36, v65, v61
	v_and_b32_e32 v61, 0xffff0000, v37
	v_lshlrev_b32_e32 v37, 16, v37
	v_add_u32_e32 v65, 0x3eb4, v104
	v_cvt_pk_bf16_f32 v78, v72, v69
	v_cvt_pk_bf16_f32 v82, v67, v68
	ds_read_b64 v[68:69], v111
	ds_read2_b32 v[70:71], v65 offset1:1
	ds_read2_b32 v[72:73], v103 offset0:14 offset1:15
	v_mul_f32_e32 v65, 0xbfb8aa3b, v37
	v_exp_f32_e32 v67, v65
	s_waitcnt lgkmcnt(2)
	v_mov_b32_e32 v65, v68
	v_pk_add_f32 v[64:65], v[64:65], 1.0 op_sel_hi:[1,0] neg_lo:[1,0] neg_hi:[1,0]
	s_waitcnt lgkmcnt(0)
	v_sub_f32_e32 v68, v72, v70
	v_mul_f32_e32 v64, v64, v65
	v_add_f32_e32 v65, 1.0, v67
	v_rcp_f32_e32 v65, v65
	v_mul_f32_e32 v67, 0x3fb8aa3b, v72
	v_mul_f32_e32 v68, 0x3fb8aa3b, v68
	v_exp_f32_e32 v67, v67
	v_exp_f32_e32 v68, v68
	v_sub_f32_e32 v70, v70, v72
	v_mul_f32_e32 v37, v65, v37
	v_mul_f32_e32 v70, 0x3fb8aa3b, v70
	v_mul_f32_e32 v72, v37, v67
	v_mul_f32_e32 v68, v37, v68
	v_mul_f32_e32 v37, 0xbfb8aa3b, v61
	v_exp_f32_e32 v70, v70
	v_exp_f32_e32 v37, v37
	v_mov_b32_e32 v67, v69
	s_add_i32 s80, s80, s28
	v_mul_f32_e32 v70, v64, v70
	v_pk_add_f32 v[64:65], v[66:67], 1.0 op_sel_hi:[1,0] neg_lo:[1,0] neg_hi:[1,0]
	v_add_f32_e32 v37, 1.0, v37
	v_sub_f32_e32 v66, v73, v71
	v_sub_f32_e32 v67, v71, v73
	v_mul_f32_e32 v64, v64, v65
	v_rcp_f32_e32 v37, v37
	v_mul_f32_e32 v65, 0x3fb8aa3b, v73
	v_mul_f32_e32 v66, 0x3fb8aa3b, v66
	v_mul_f32_e32 v67, 0x3fb8aa3b, v67
	v_exp_f32_e32 v65, v65
	v_exp_f32_e32 v66, v66
	v_exp_f32_e32 v67, v67
	v_mul_f32_e32 v37, v37, v61
	v_mul_f32_e32 v61, v37, v65
	v_mul_f32_e32 v65, v37, v66
	v_mul_f32_e32 v64, v64, v67
	v_cvt_pk_bf16_f32 v37, v72, v61
	v_cvt_pk_bf16_f32 v79, v68, v65
	v_cvt_pk_bf16_f32 v83, v70, v64
	ds_write_b128 v117, v[46:49] offset:33792
	ds_write_b128 v117, v[34:37] offset:33808
	ds_write_b128 v117, v[42:45] offset:51200
	ds_write_b128 v117, v[76:79] offset:51216
	ds_write_b128 v118, v[38:41]
	ds_write_b128 v118, v[80:83] offset:16
	s_waitcnt vmcnt(5)
	v_and_b32_e32 v34, 0xffff, v26
	v_lshrrev_b32_e32 v26, 16, v26
	s_waitcnt vmcnt(4)
	v_lshl_or_b32 v34, v30, 16, v34
	v_and_or_b32 v26, v30, s58, v26
	ds_write2_b32 v119, v34, v26 offset1:36
	v_and_b32_e32 v26, 0xffff, v27
	v_lshrrev_b32_e32 v27, 16, v27
	v_lshl_or_b32 v26, v31, 16, v26
	v_and_or_b32 v27, v31, s58, v27
	ds_write2_b32 v119, v26, v27 offset0:72 offset1:108
	v_and_b32_e32 v26, 0xffff, v28
	v_lshrrev_b32_e32 v27, 16, v28
	v_lshl_or_b32 v26, v32, 16, v26
	v_and_or_b32 v27, v32, s58, v27
	ds_write2_b32 v119, v26, v27 offset0:144 offset1:180
	v_and_b32_e32 v26, 0xffff, v29
	v_lshl_or_b32 v26, v33, 16, v26
	ds_write_b32 v119, v26 offset:864
	v_lshrrev_b32_e32 v26, 16, v29
	v_and_or_b32 v26, v33, s58, v26
	ds_write_b32 v120, v26
	s_waitcnt lgkmcnt(0)
	s_barrier
	ds_read_b128 v[26:29], v121 offset:51200
	v_add_u32_e32 v42, v113, v112
	ds_read_b128 v[30:33], v121 offset:51264
	ds_read_b128 v[34:37], v42
	ds_read_b128 v[38:41], v42 offset:64
	s_waitcnt lgkmcnt(1)
	v_mfma_f32_16x16x32_bf16 v[26:29], v[26:29], v[34:37], 0
	ds_read_b128 v[34:37], v121 offset:51328
	v_add_u32_e32 v46, v114, v94
	v_and_b32_e32 v48, 0xffff0000, v8
	s_waitcnt lgkmcnt(1)
	v_mfma_f32_16x16x32_bf16 v[26:29], v[30:33], v[38:41], v[26:29]
	ds_read_b128 v[30:33], v121 offset:51392
	ds_read_b128 v[38:41], v42 offset:128
	ds_read_b128 v[42:45], v42 offset:192
	v_lshlrev_b32_e32 v8, 16, v8
	s_cmpk_gt_i32 s80, 0x7ff
	s_waitcnt lgkmcnt(1)
	v_mfma_f32_16x16x32_bf16 v[26:29], v[34:37], v[38:41], v[26:29]
	s_waitcnt lgkmcnt(0)
	v_mfma_f32_16x16x32_bf16 v[26:29], v[30:33], v[42:45], v[26:29]
	s_nop 7
	v_cndmask_b32_e64 v26, v26, 0, s[6:7]
	v_bfe_u32 v30, v26, 16, 1
	v_add3_u32 v26, v26, v30, s59
	ds_write_b16_d16_hi v122, v26
	v_cndmask_b32_e64 v26, v27, 0, s[8:9]
	v_bfe_u32 v27, v26, 16, 1
	v_add3_u32 v26, v26, v27, s59
	ds_write_b16_d16_hi v122, v26 offset:144
	v_cndmask_b32_e64 v26, v28, 0, s[10:11]
	v_bfe_u32 v27, v26, 16, 1
	v_add3_u32 v26, v26, v27, s59
	ds_write_b16_d16_hi v122, v26 offset:288
	v_cndmask_b32_e64 v26, v29, 0, s[12:13]
	v_bfe_u32 v27, v26, 16, 1
	v_add3_u32 v26, v26, v27, s59
	ds_write_b16_d16_hi v122, v26 offset:432
	ds_read_b128 v[26:29], v121 offset:51200
	ds_read_b128 v[30:33], v121 offset:51264
	ds_read_b128 v[34:37], v123
	ds_read_b128 v[38:41], v123 offset:64
	s_waitcnt lgkmcnt(1)
	v_mfma_f32_16x16x32_bf16 v[26:29], v[26:29], v[34:37], 0
	ds_read_b128 v[34:37], v121 offset:51328
	s_waitcnt lgkmcnt(1)
	v_mfma_f32_16x16x32_bf16 v[26:29], v[30:33], v[38:41], v[26:29]
	ds_read_b128 v[30:33], v121 offset:51392
	ds_read_b128 v[38:41], v123 offset:128
	ds_read_b128 v[42:45], v123 offset:192
	s_waitcnt lgkmcnt(1)
	v_mfma_f32_16x16x32_bf16 v[26:29], v[34:37], v[38:41], v[26:29]
	s_waitcnt lgkmcnt(0)
	v_mfma_f32_16x16x32_bf16 v[26:29], v[30:33], v[42:45], v[26:29]
	s_nop 7
	v_cndmask_b32_e64 v26, v26, 0, s[14:15]
	v_bfe_u32 v30, v26, 16, 1
	v_add3_u32 v26, v26, v30, s59
	ds_write_b16_d16_hi v124, v26
	v_cndmask_b32_e64 v26, v27, 0, s[16:17]
	v_bfe_u32 v27, v26, 16, 1
	v_add3_u32 v26, v26, v27, s59
	ds_write_b16_d16_hi v124, v26 offset:144
	v_cndmask_b32_e64 v26, v28, 0, s[18:19]
	v_bfe_u32 v27, v26, 16, 1
	v_add3_u32 v26, v26, v27, s59
	ds_write_b16_d16_hi v124, v26 offset:288
	v_cndmask_b32_e64 v26, v29, 0, s[20:21]
	v_bfe_u32 v27, v26, 16, 1
	v_add3_u32 v26, v26, v27, s59
	ds_write_b16_d16_hi v124, v26 offset:432
	s_waitcnt lgkmcnt(0)
	s_barrier
	ds_read_b128 v[26:29], v126
	ds_read_b128 v[30:33], v125
	ds_read_b128 v[34:37], v126 offset:64
	ds_read_b128 v[38:41], v125 offset:64
	s_waitcnt lgkmcnt(2)
	v_mfma_f32_16x16x32_bf16 v[26:29], v[26:29], v[30:33], 0
	ds_read_b128 v[42:45], v46 offset:33792
	s_waitcnt lgkmcnt(1)
	v_mfma_f32_16x16x32_bf16 v[26:29], v[34:37], v[38:41], v[26:29]
	ds_read_b128 v[34:37], v46 offset:33856
	s_waitcnt vmcnt(3) lgkmcnt(1)
	v_mfma_f32_16x16x32_bf16 v[26:29], v[42:45], v[22:25], v[26:29]
	ds_read_b128 v[42:45], v46 offset:33920
	s_waitcnt vmcnt(2) lgkmcnt(1)
	v_mfma_f32_16x16x32_bf16 v[26:29], v[34:37], v[18:21], v[26:29]
	ds_read_b128 v[34:37], v46 offset:33984
	s_waitcnt vmcnt(1) lgkmcnt(1)
	v_mfma_f32_16x16x32_bf16 v[26:29], v[42:45], v[10:13], v[26:29]
	s_waitcnt vmcnt(0) lgkmcnt(0)
	v_mfma_f32_16x16x32_bf16 v[26:29], v[34:37], v[14:17], v[26:29]
	s_nop 7
	ds_write2_b32 v127, v26, v27 offset1:132
	v_add_u32_e32 v26, 0x400, v127
	ds_write2_b32 v26, v28, v29 offset0:8 offset1:140
	ds_read_b128 v[26:29], v126 offset:2304
	ds_read_b128 v[34:37], v126 offset:2368
	s_waitcnt lgkmcnt(1)
	v_mfma_f32_16x16x32_bf16 v[26:29], v[26:29], v[30:33], 0
	ds_read_b128 v[42:45], v46 offset:38144
	s_waitcnt lgkmcnt(1)
	v_mfma_f32_16x16x32_bf16 v[26:29], v[34:37], v[38:41], v[26:29]
	ds_read_b128 v[34:37], v46 offset:38208
	s_waitcnt lgkmcnt(1)
	v_mfma_f32_16x16x32_bf16 v[26:29], v[42:45], v[22:25], v[26:29]
	ds_read_b128 v[42:45], v46 offset:38272
	s_waitcnt lgkmcnt(1)
	v_mfma_f32_16x16x32_bf16 v[26:29], v[34:37], v[18:21], v[26:29]
	ds_read_b128 v[34:37], v46 offset:38336
	s_waitcnt lgkmcnt(1)
	v_mfma_f32_16x16x32_bf16 v[26:29], v[42:45], v[10:13], v[26:29]
	s_waitcnt lgkmcnt(0)
	v_mfma_f32_16x16x32_bf16 v[26:29], v[34:37], v[14:17], v[26:29]
	v_add_u32_e32 v34, 0x2000, v127
	s_nop 6
	ds_write2_b32 v34, v26, v27 offset0:64 offset1:196
	v_add_u32_e32 v26, 0x2400, v127
	ds_write2_b32 v26, v28, v29 offset0:72 offset1:204
	ds_read_b128 v[26:29], v126 offset:4608
	ds_read_b128 v[34:37], v126 offset:4672
	s_waitcnt lgkmcnt(1)
	v_mfma_f32_16x16x32_bf16 v[26:29], v[26:29], v[30:33], 0
	ds_read_b128 v[42:45], v46 offset:42496
	s_waitcnt lgkmcnt(1)
	v_mfma_f32_16x16x32_bf16 v[26:29], v[34:37], v[38:41], v[26:29]
	ds_read_b128 v[34:37], v46 offset:42560
	s_waitcnt lgkmcnt(1)
	v_mfma_f32_16x16x32_bf16 v[26:29], v[42:45], v[22:25], v[26:29]
	ds_read_b128 v[42:45], v46 offset:42624
	s_waitcnt lgkmcnt(1)
	v_mfma_f32_16x16x32_bf16 v[26:29], v[34:37], v[18:21], v[26:29]
	ds_read_b128 v[34:37], v46 offset:42688
	s_waitcnt lgkmcnt(1)
	v_mfma_f32_16x16x32_bf16 v[26:29], v[42:45], v[10:13], v[26:29]
	v_lshlrev_b32_e32 v44, 16, v9
	v_and_b32_e32 v42, 0xffff0000, v9
	v_mul_f32_e32 v9, 0xbfb8aa3b, v44
	s_waitcnt lgkmcnt(0)
	v_mfma_f32_16x16x32_bf16 v[26:29], v[34:37], v[14:17], v[26:29]
	v_add_u32_e32 v34, 0x4200, v127
	v_exp_f32_e32 v9, v9
	s_nop 0
	v_add_f32_e32 v9, 1.0, v9
	v_rcp_f32_e32 v46, v9
	s_nop 2
	ds_write2_b32 v34, v26, v27 offset1:132
	v_add_u32_e32 v26, 0x4600, v127
	ds_write2_b32 v26, v28, v29 offset0:8 offset1:140
	ds_read_b128 v[26:29], v128
	ds_read_b128 v[34:37], v128 offset:64
	s_waitcnt lgkmcnt(1)
	v_mfma_f32_16x16x32_bf16 v[26:29], v[26:29], v[30:33], 0
	ds_read_b128 v[30:33], v129 offset:33792
	v_mul_f32_e32 v9, 0xbfb8aa3b, v48
	v_exp_f32_e32 v9, v9
	s_waitcnt lgkmcnt(1)
	v_mfma_f32_16x16x32_bf16 v[26:29], v[34:37], v[38:41], v[26:29]
	ds_read_b128 v[34:37], v129 offset:33856
	v_add_f32_e32 v9, 1.0, v9
	s_waitcnt lgkmcnt(1)
	v_mfma_f32_16x16x32_bf16 v[22:25], v[30:33], v[22:25], v[26:29]
	s_nop 3
	ds_read_b128 v[26:29], v129 offset:33920
	s_waitcnt lgkmcnt(1)
	v_mfma_f32_16x16x32_bf16 v[18:21], v[34:37], v[18:21], v[22:25]
	s_nop 2
	ds_read_b128 v[22:25], v129 offset:33984
	s_waitcnt lgkmcnt(1)
	v_mfma_f32_16x16x32_bf16 v[10:13], v[26:29], v[10:13], v[18:21]
	s_waitcnt lgkmcnt(0)
	v_mfma_f32_16x16x32_bf16 v[10:13], v[22:25], v[14:17], v[10:13]
	v_add_u32_e32 v14, 0x6200, v127
	s_nop 6
	ds_write2_b32 v14, v10, v11 offset0:64 offset1:196
	v_add_u32_e32 v10, 0x6600, v127
	ds_write2_b32 v10, v12, v13 offset0:72 offset1:204
	s_waitcnt lgkmcnt(0)
	s_barrier
	v_mov_b32_e32 v10, v238
	v_mov_b32_e32 v11, v239
	v_mov_b32_e32 v12, v240
	v_mov_b32_e32 v13, v241
	ds_read_b128 v[18:21], v115
	ds_read_b128 v[22:25], v115 offset:16
	ds_read_b128 v[26:29], v115 offset:32
	ds_read_b128 v[14:17], v115 offset:48
	s_waitcnt lgkmcnt(3)
	v_mul_f32_e32 v32, v19, v19
	v_fmac_f32_e32 v32, v18, v18
	v_fmac_f32_e32 v32, v20, v20
	v_fmac_f32_e32 v32, v21, v21
	s_waitcnt lgkmcnt(2)
	v_fmac_f32_e32 v32, v22, v22
	v_fmac_f32_e32 v32, v23, v23
	v_fmac_f32_e32 v32, v24, v24
	v_fmac_f32_e32 v32, v25, v25
	s_waitcnt lgkmcnt(1)
	v_pk_mul_f32 v[30:31], v[26:27], v[26:27]
	s_waitcnt lgkmcnt(0)
	v_pk_mul_f32 v[34:35], v[16:17], v[16:17]
	v_add_f32_e32 v30, v32, v30
	v_add_f32_e32 v32, v30, v31
	v_pk_mul_f32 v[30:31], v[28:29], v[28:29]
	v_mov_b32_e32 v49, v11
	v_add_f32_e32 v30, v32, v30
	v_add_f32_e32 v32, v30, v31
	v_pk_mul_f32 v[30:31], v[14:15], v[14:15]
	s_nop 0
	v_add_f32_e32 v30, v32, v30
	v_add_f32_e32 v36, v30, v31
	v_mov_b32_e32 v30, v242
	v_mov_b32_e32 v31, v243
	v_mov_b32_e32 v32, v244
	v_mov_b32_e32 v33, v245
	v_add_f32_e32 v34, v36, v34
	v_and_b32_e32 v36, 64, v134
	v_add_f32_e32 v34, v34, v35
	v_xor_b32_e32 v35, 1, v134
	v_add_u32_e32 v36, 64, v36
	v_cmp_lt_i32_e32 vcc, v35, v36
	s_nop 1
	v_cndmask_b32_e32 v35, v134, v35, vcc
	v_lshlrev_b32_e32 v35, 2, v35
	ds_bpermute_b32 v35, v35, v34
	s_waitcnt lgkmcnt(0)
	v_add_f32_e32 v34, v34, v35
	v_xor_b32_e32 v35, 2, v134
	v_cmp_lt_i32_e32 vcc, v35, v36
	s_nop 1
	v_cndmask_b32_e32 v35, v134, v35, vcc
	v_lshlrev_b32_e32 v35, 2, v35
	ds_bpermute_b32 v35, v35, v34
	s_waitcnt lgkmcnt(0)
	v_add_f32_e32 v38, v34, v35
	v_xor_b32_e32 v34, 4, v134
	v_cmp_lt_i32_e32 vcc, v34, v36
	s_nop 1
	v_cndmask_b32_e32 v34, v134, v34, vcc
	v_lshlrev_b32_e32 v34, 2, v34
	ds_bpermute_b32 v39, v34, v38
	v_mov_b32_e32 v34, v246
	v_mov_b32_e32 v35, v247
	v_mov_b32_e32 v36, v248
	v_mov_b32_e32 v37, v249
	s_waitcnt lgkmcnt(0)
	v_add_f32_e32 v38, v38, v39
	v_fmamk_f32 v38, v38, 0x3c000000, v130
	v_mul_f32_e32 v39, 0x4b800000, v38
	v_cmp_gt_f32_e32 vcc, s54, v38
	s_nop 1
	v_cndmask_b32_e32 v38, v38, v39, vcc
	v_rsq_f32_e32 v43, v38
	v_mov_b32_e32 v38, v250
	v_mov_b32_e32 v39, v251
	v_mov_b32_e32 v40, v252
	v_mov_b32_e32 v41, v253
	v_mul_f32_e32 v45, 0x45800000, v43
	v_cndmask_b32_e32 v43, v43, v45, vcc
	v_mul_f32_e32 v43, 0x41800000, v43
	v_mul_f32_e32 v47, v16, v43
	v_mov_b32_e32 v45, v12
	v_pk_mul_f32 v[44:45], v[46:47], v[44:45]
	s_nop 0
	v_mul_f32_e32 v12, v44, v45
	v_rcp_f32_e32 v44, v9
	v_mul_f32_e32 v9, 0xbfb8aa3b, v8
	v_exp_f32_e32 v9, v9
	v_mul_f32_e32 v45, v15, v43
	v_mul_f32_e32 v15, v14, v43
	v_pk_mul_f32 v[44:45], v[44:45], v[48:49]
	v_add_f32_e32 v9, 1.0, v9
	v_rcp_f32_e32 v14, v9
	v_mov_b32_e32 v9, v10
	v_and_b32_e32 v10, 0xffff0000, v7
	v_mul_f32_e32 v11, 0xbfb8aa3b, v10
	v_exp_f32_e32 v11, v11
	v_pk_mul_f32 v[8:9], v[14:15], v[8:9]
	v_lshlrev_b32_e32 v14, 16, v7
	v_mul_f32_e32 v16, v44, v45
	v_mul_f32_e32 v44, v8, v9
	v_add_f32_e32 v8, 1.0, v11
	v_mul_f32_e32 v7, 0xbfb8aa3b, v14
	v_rcp_f32_e32 v8, v8
	v_exp_f32_e32 v7, v7
	v_mul_f32_e32 v9, v29, v43
	v_mov_b32_e32 v11, v33
	v_pk_mul_f32 v[8:9], v[8:9], v[10:11]
	v_add_f32_e32 v7, 1.0, v7
	v_and_b32_e32 v10, 0xffff0000, v6
	v_mul_f32_e32 v29, v8, v9
	v_rcp_f32_e32 v8, v7
	v_mul_f32_e32 v7, 0xbfb8aa3b, v10
	v_exp_f32_e32 v7, v7
	v_mul_f32_e32 v9, v28, v43
	v_mov_b32_e32 v15, v32
	v_pk_mul_f32 v[8:9], v[8:9], v[14:15]
	v_add_f32_e32 v7, 1.0, v7
	v_lshlrev_b32_e32 v6, 16, v6
	v_mul_f32_e32 v14, v8, v9
	v_rcp_f32_e32 v8, v7
	v_mul_f32_e32 v7, 0xbfb8aa3b, v6
	v_exp_f32_e32 v15, v7
	v_mul_f32_e32 v11, v27, v43
	v_mov_b32_e32 v9, v31
	v_pk_mul_f32 v[8:9], v[8:9], v[10:11]
	v_and_b32_e32 v10, 0xffff0000, v5
	v_mul_f32_e32 v27, v8, v9
	v_add_f32_e32 v8, 1.0, v15
	v_rcp_f32_e32 v8, v8
	v_mul_f32_e32 v11, 0xbfb8aa3b, v10
	v_exp_f32_e32 v15, v11
	v_mul_f32_e32 v7, v26, v43
	v_mov_b32_e32 v9, v30
	v_pk_mul_f32 v[6:7], v[8:9], v[6:7]
	v_lshlrev_b32_e32 v8, 16, v5
	v_mul_f32_e32 v26, v6, v7
	v_add_f32_e32 v6, 1.0, v15
	v_mul_f32_e32 v5, 0xbfb8aa3b, v8
	v_rcp_f32_e32 v6, v6
	v_exp_f32_e32 v5, v5
	v_mul_f32_e32 v11, v25, v43
	v_mov_b32_e32 v7, v37
	v_pk_mul_f32 v[6:7], v[6:7], v[10:11]
	v_add_f32_e32 v5, 1.0, v5
	v_and_b32_e32 v10, 0xffff0000, v4
	v_mul_f32_e32 v15, v6, v7
	v_rcp_f32_e32 v6, v5
	v_mul_f32_e32 v5, 0xbfb8aa3b, v10
	v_exp_f32_e32 v5, v5
	v_mul_f32_e32 v9, v24, v43
	v_mov_b32_e32 v7, v36
	v_pk_mul_f32 v[6:7], v[6:7], v[8:9]
	v_add_f32_e32 v5, 1.0, v5
	v_lshlrev_b32_e32 v4, 16, v4
	v_mul_f32_e32 v24, v6, v7
	v_rcp_f32_e32 v6, v5
	v_mul_f32_e32 v5, 0xbfb8aa3b, v4
	v_exp_f32_e32 v8, v5
	v_mul_f32_e32 v11, v23, v43
	v_mov_b32_e32 v7, v35
	v_pk_mul_f32 v[6:7], v[6:7], v[10:11]
	v_mul_f32_e32 v5, v22, v43
	v_mul_f32_e32 v10, v6, v7
	v_add_f32_e32 v6, 1.0, v8
	v_and_b32_e32 v8, 0xffff0000, v3
	v_rcp_f32_e32 v6, v6
	v_mul_f32_e32 v9, 0xbfb8aa3b, v8
	v_exp_f32_e32 v11, v9
	v_mov_b32_e32 v7, v34
	v_pk_mul_f32 v[4:5], v[6:7], v[4:5]
	v_lshlrev_b32_e32 v6, 16, v3
	v_mul_f32_e32 v22, v4, v5
	v_add_f32_e32 v4, 1.0, v11
	v_mul_f32_e32 v3, 0xbfb8aa3b, v6
	v_rcp_f32_e32 v4, v4
	v_exp_f32_e32 v3, v3
	v_mul_f32_e32 v9, v21, v43
	v_mov_b32_e32 v5, v41
	v_pk_mul_f32 v[4:5], v[4:5], v[8:9]
	v_add_f32_e32 v3, 1.0, v3
	v_and_b32_e32 v8, 0xffff0000, v2
	v_mul_f32_e32 v11, v4, v5
	v_rcp_f32_e32 v4, v3
	v_mul_f32_e32 v3, 0xbfb8aa3b, v8
	v_exp_f32_e32 v3, v3
	v_mul_f32_e32 v7, v20, v43
	v_mov_b32_e32 v5, v40
	v_pk_mul_f32 v[4:5], v[4:5], v[6:7]
	v_add_f32_e32 v3, 1.0, v3
	v_lshlrev_b32_e32 v2, 16, v2
	v_mul_f32_e32 v6, v4, v5
	v_rcp_f32_e32 v4, v3
	v_mul_f32_e32 v3, 0xbfb8aa3b, v2
	v_exp_f32_e32 v3, v3
	v_mul_f32_e32 v9, v19, v43
	v_mov_b32_e32 v5, v39
	v_pk_mul_f32 v[4:5], v[4:5], v[8:9]
	v_add_f32_e32 v3, 1.0, v3
	v_mul_f32_e32 v7, v4, v5
	v_rcp_f32_e32 v4, v3
	v_mul_f32_e32 v3, 0xbfb8aa3b, v42
	v_exp_f32_e32 v8, v3
	v_mul_f32_e32 v3, v18, v43
	v_mov_b32_e32 v5, v38
	v_pk_mul_f32 v[2:3], v[4:5], v[2:3]
	v_add_f32_e32 v4, 1.0, v8
	v_rcp_f32_e32 v4, v4
	v_mul_f32_e32 v5, v17, v43
	v_mov_b32_e32 v43, v13
	v_mul_f32_e32 v8, v2, v3
	v_pk_mul_f32 v[2:3], v[4:5], v[42:43]
	v_mov_b32_e32 v4, v55
	v_mul_f32_e32 v9, v2, v3
	v_mov_b32_e32 v2, v55
	v_mov_b32_e32 v3, v55
	v_mov_b32_e32 v5, v55
	v_cvt_pk_fp8_f32 v2, v8, v7
	v_cvt_pk_fp8_f32 v3, v22, v10
	v_cvt_pk_fp8_f32 v4, v26, v27
	v_cvt_pk_fp8_f32 v5, v44, v16
	v_cvt_pk_fp8_f32 v2, v6, v11 op_sel:[0,0,1]
	v_cvt_pk_fp8_f32 v3, v24, v15 op_sel:[0,0,1]
	v_cvt_pk_fp8_f32 v4, v14, v29 op_sel:[0,0,1]
	v_cvt_pk_fp8_f32 v5, v12, v9 op_sel:[0,0,1]
	v_lshlrev_b64 v[6:7], 10, v[62:63]
	v_lshl_add_u64 v[6:7], s[26:27], 0, v[6:7]
	v_lshl_add_u64 v[6:7], v[6:7], 0, s[60:61]
	v_lshl_add_u64 v[6:7], v[6:7], 0, v[52:53]
	global_store_dwordx4 v[6:7], v[2:5], off
	s_barrier
	s_cbranch_scc1 .LBB0_508
